# speedup vs baseline: 1.0238x; 1.0238x over previous
_Z12score_kernelPKfP15HIP_vector_typeIjLj2EES0_S0_:
	s_load_dwordx4 s[4:7], s[0:1], 0x0
	s_load_dwordx4 s[32:35], s[0:1], 0x10
	v_readfirstlane_b32 s21, v0
	s_cmp_lg_u32 s21, 0
	s_cbranch_scc1 .Lk1_nowarm0
	s_getpc_b64 s[30:31]
	v_lshlrev_b32_e32 v3, 6, v0
	global_load_dword v92, v3, s[30:31]
	s_add_u32 s30, s30, 0x1000
	s_addc_u32 s31, s31, 0
	global_load_dword v93, v3, s[30:31]
	s_add_u32 s30, s30, 0x1000
	s_addc_u32 s31, s31, 0
	global_load_dword v94, v3, s[30:31]
	s_and_b32 s30, s0, 0xfffff000
	s_mov_b32 s31, s1
	global_load_dword v95, v3, s[30:31]
.Lk1_nowarm0:
	s_and_b32 s15, s2, 7
	s_lshl_b32 s15, s15, 2
	s_lshr_b32 s17, s2, 6
	s_add_u32 s15, s15, s17
	s_bfe_u32 s16, s2, 0x30003
	s_mul_i32 s17, s16, 0x271
	v_add_u32_e32 v2, s17, v0
	v_lshlrev_b32_e32 v1, 2, v2
	s_movk_i32 s17, 0x271
	v_cmp_gt_u32_e32 vcc, s17, v0
	s_and_b64 exec, exec, vcc
	s_mov_b64 s[18:19], exec
	s_lshr_b32 s21, s21, 6
	s_movk_i32 s13, 0x4e20
	s_mov_b32 s14, 0x3fb8aa3b
	s_mov_b32 s12, 0
	s_mov_b32 s10, 0x13d620
	s_mov_b32 s11, 0x20000
	s_mul_i32 s17, s15, 0x13d620
	s_mul_hi_u32 s20, s15, 0x13d620
	s_mov_b32 s40, 0
	s_add_u32 s41, s40, s13
	s_add_u32 s42, s41, s13
	s_add_u32 s43, s42, s13
	s_add_u32 s44, s43, s13
	s_add_u32 s45, s44, s13
	s_add_u32 s46, s45, s13
	s_add_u32 s47, s46, s13
	s_add_u32 s48, s47, s13
	s_add_u32 s49, s48, s13
	s_add_u32 s50, s49, s13
	s_add_u32 s51, s50, s13
	s_add_u32 s52, s51, s13
	s_add_u32 s53, s52, s13
	s_add_u32 s54, s53, s13
	s_add_u32 s55, s54, s13
	s_waitcnt lgkmcnt(0)
	s_add_u32 s8, s4, s17
	s_addc_u32 s9, s5, s20
	s_and_b32 s9, s9, 0xffff
	s_cmp_eq_u32 s21, 9
	s_cselect_b32 s17, 1, 0
	s_cmp_eq_u32 s16, 0
	s_cselect_b32 s17, s17, 0
	s_cmp_lg_u32 s17, 0
	s_cbranch_scc0 .Lk1_nowarm9
	s_mul_i32 s22, s15, 0x3a9800
	v_writelane_b32 v3, s22, 0
	s_add_u32 s23, s22, 0x10000
	v_writelane_b32 v3, s23, 1
	s_add_u32 s22, s22, 0x138800
	v_writelane_b32 v3, s22, 2
	s_add_u32 s23, s22, 0x10000
	v_writelane_b32 v3, s23, 3
	s_add_u32 s22, s22, 0x138800
	v_writelane_b32 v3, s22, 4
	s_add_u32 s23, s22, 0x10000
	v_writelane_b32 v3, s23, 5
	s_mov_b64 exec, 63
	global_load_dword v92, v3, s[32:33]
	s_mul_i32 s22, s15, 0x12c00
	s_add_u32 s22, s22, 0x1c200
	v_writelane_b32 v3, s22, 0
	s_add_u32 s22, s22, 0x10000
	v_writelane_b32 v3, s22, 1
	s_mul_i32 s22, s15, 0xe10
	v_writelane_b32 v3, s22, 2
	s_mul_i32 s22, s15, 0x4b0
	s_add_u32 s22, s22, 0x274200
	v_writelane_b32 v3, s22, 3
	s_mov_b64 exec, 15
	global_load_dword v93, v3, s[34:35]
	s_mov_b64 exec, s[18:19]
